# v40 + early L2 write-back: the workgroups arriving with 16 and 4 peers outstanding at an XCD barrier counter issue an extra buffer_wbl2 before spinning
# baseline (speedup 1.0000x reference)
.LBB0_241:
	s_lshl_b32 s18, s33, 6
	s_add_i32 s92, s18, 0x500
	s_lshl_b64 s[0:1], s[92:93], 2
	v_lshl_add_u64 v[8:9], v[4:5], 0, s[0:1]
	v_mov_b32_e32 v1, 1
	flat_atomic_add v1, v[8:9], v1 sc0
	v_cvt_f32_u32_e32 v7, v6
	v_sub_u32_e32 v8, 0, v6
	v_rcp_iflag_f32_e32 v7, v7
	s_nop 0
	v_mul_f32_e32 v7, 0x4f7ffffe, v7
	v_cvt_u32_f32_e32 v7, v7
	v_mul_lo_u32 v8, v8, v7
	v_mul_hi_u32 v8, v7, v8
	v_add_u32_e32 v7, v7, v8
	s_waitcnt vmcnt(0) lgkmcnt(0)
	v_mul_hi_u32 v7, v1, v7
	v_mul_lo_u32 v9, v7, v6
	v_add_u32_e32 v8, 1, v1
	v_sub_u32_e32 v1, v1, v9
	v_add_u32_e32 v10, 1, v7
	v_cmp_ge_u32_e32 vcc, v1, v6
	v_sub_u32_e32 v9, v1, v6
	s_nop 0
	v_cndmask_b32_e32 v7, v7, v10, vcc
	v_cndmask_b32_e32 v1, v1, v9, vcc
	v_add_u32_e32 v9, 1, v7
	v_cmp_ge_u32_e32 vcc, v1, v6
	s_nop 1
	v_cndmask_b32_e32 v1, v7, v9, vcc
	v_mad_u64_u32 v[6:7], s[0:1], v6, v1, v[6:7]
	v_cmp_ne_u32_e32 vcc, v8, v6
	s_and_saveexec_b64 s[0:1], vcc
	s_xor_b64 s[0:1], exec, s[0:1]
	s_cbranch_execz .LBB0_254
	v_sub_u32_e32 v2, v6, v8
	v_lshlrev_b32_e64 v2, v2, 1
	v_and_b32_e32 v2, 0x10010, v2
	v_cmp_ne_u32_e32 vcc, 0, v2
	s_cbranch_vccz .Lewb_1
	buffer_wbl2 sc1
.Lewb_1:
	s_add_i32 s92, s18, 0x900
	s_lshl_b64 s[2:3], s[92:93], 2
	v_lshl_add_u64 v[6:7], v[4:5], 0, s[2:3]
	flat_load_dword v2, v[6:7] sc1
	s_waitcnt vmcnt(0) lgkmcnt(0)
	v_cmp_eq_u32_e32 vcc, v2, v1
	s_and_saveexec_b64 s[2:3], vcc
	s_cbranch_execz .LBB0_253
	s_mov_b32 s19, 1
	s_mov_b64 s[4:5], 0
	s_branch .LBB0_245

.LBB0_483:
	s_lshl_b32 s18, s34, 6
	s_add_i32 s92, s18, 0x500
	s_lshl_b64 s[0:1], s[92:93], 2
	v_lshl_add_u64 v[8:9], v[4:5], 0, s[0:1]
	v_mov_b32_e32 v1, 1
	flat_atomic_add v7, v[8:9], v1 sc0
	v_cvt_f32_u32_e32 v1, v6
	v_sub_u32_e32 v8, 0, v6
	v_rcp_iflag_f32_e32 v1, v1
	s_nop 0
	v_mul_f32_e32 v1, 0x4f7ffffe, v1
	v_cvt_u32_f32_e32 v1, v1
	v_mul_lo_u32 v8, v8, v1
	v_mul_hi_u32 v8, v1, v8
	v_add_u32_e32 v1, v1, v8
	s_waitcnt vmcnt(0) lgkmcnt(0)
	v_mul_hi_u32 v1, v7, v1
	v_mul_lo_u32 v8, v1, v6
	v_sub_u32_e32 v8, v7, v8
	v_cmp_ge_u32_e32 vcc, v8, v6
	v_add_u32_e32 v9, 1, v1
	s_nop 0
	v_cndmask_b32_e32 v1, v1, v9, vcc
	v_sub_u32_e32 v9, v8, v6
	v_cndmask_b32_e32 v8, v8, v9, vcc
	v_cmp_ge_u32_e32 vcc, v8, v6
	v_add_u32_e32 v8, 1, v1
	s_nop 0
	v_cndmask_b32_e32 v1, v1, v8, vcc
	v_add_u32_e32 v8, 1, v7
	v_mad_u64_u32 v[6:7], s[0:1], v6, v1, v[6:7]
	v_cmp_ne_u32_e32 vcc, v8, v6
	s_and_saveexec_b64 s[0:1], vcc
	s_xor_b64 s[0:1], exec, s[0:1]
	s_cbranch_execz .LBB0_496
	v_sub_u32_e32 v2, v6, v8
	v_lshlrev_b32_e64 v2, v2, 1
	v_and_b32_e32 v2, 0x10010, v2
	v_cmp_ne_u32_e32 vcc, 0, v2
	s_cbranch_vccz .Lewb_2
	buffer_wbl2 sc1

.LBB0_1095:
	s_lshl_b32 s20, s33, 6
	s_add_i32 s92, s20, 0x500
	s_lshl_b64 s[0:1], s[92:93], 2
	v_lshl_add_u64 v[8:9], v[4:5], 0, s[0:1]
	v_mov_b32_e32 v1, 1
	flat_atomic_add v7, v[8:9], v1 sc0
	v_cvt_f32_u32_e32 v1, v6
	v_sub_u32_e32 v8, 0, v6
	v_rcp_iflag_f32_e32 v1, v1
	s_nop 0
	v_mul_f32_e32 v1, 0x4f7ffffe, v1
	v_cvt_u32_f32_e32 v1, v1
	v_mul_lo_u32 v8, v8, v1
	v_mul_hi_u32 v8, v1, v8
	v_add_u32_e32 v1, v1, v8
	s_waitcnt vmcnt(0) lgkmcnt(0)
	v_mul_hi_u32 v1, v7, v1
	v_mul_lo_u32 v8, v1, v6
	v_sub_u32_e32 v8, v7, v8
	v_cmp_ge_u32_e32 vcc, v8, v6
	v_add_u32_e32 v9, 1, v1
	s_nop 0
	v_cndmask_b32_e32 v1, v1, v9, vcc
	v_sub_u32_e32 v9, v8, v6
	v_cndmask_b32_e32 v8, v8, v9, vcc
	v_cmp_ge_u32_e32 vcc, v8, v6
	v_add_u32_e32 v8, 1, v1
	s_nop 0
	v_cndmask_b32_e32 v1, v1, v8, vcc
	v_add_u32_e32 v8, 1, v7
	v_mad_u64_u32 v[6:7], s[0:1], v6, v1, v[6:7]
	v_cmp_ne_u32_e32 vcc, v8, v6
	s_and_saveexec_b64 s[0:1], vcc
	s_xor_b64 s[0:1], exec, s[0:1]
	s_cbranch_execz .LBB0_1108
	v_sub_u32_e32 v2, v6, v8
	v_lshlrev_b32_e64 v2, v2, 1
	v_and_b32_e32 v2, 0x10010, v2
	v_cmp_ne_u32_e32 vcc, 0, v2
	s_cbranch_vccz .Lewb_6
	buffer_wbl2 sc1
.Lewb_6:
	s_add_i32 s92, s20, 0x900
	s_lshl_b64 s[4:5], s[92:93], 2
	v_lshl_add_u64 v[6:7], v[4:5], 0, s[4:5]
	flat_load_dword v2, v[6:7] sc1
	s_waitcnt vmcnt(0) lgkmcnt(0)
	v_cmp_eq_u32_e32 vcc, v2, v1
	s_and_saveexec_b64 s[4:5], vcc
	s_cbranch_execz .LBB0_1107
	s_mov_b32 s21, 1
	s_mov_b64 s[6:7], 0
	s_branch .LBB0_1099

.LBB0_1358:
	s_lshl_b32 s18, s33, 6
	s_add_i32 s92, s18, 0x500
	s_lshl_b64 s[0:1], s[92:93], 2
	v_lshl_add_u64 v[8:9], v[4:5], 0, s[0:1]
	v_mov_b32_e32 v1, 1
	flat_atomic_add v7, v[8:9], v1 sc0
	v_cvt_f32_u32_e32 v1, v6
	v_sub_u32_e32 v8, 0, v6
	v_rcp_iflag_f32_e32 v1, v1
	s_nop 0
	v_mul_f32_e32 v1, 0x4f7ffffe, v1
	v_cvt_u32_f32_e32 v1, v1
	v_mul_lo_u32 v8, v8, v1
	v_mul_hi_u32 v8, v1, v8
	v_add_u32_e32 v1, v1, v8
	s_waitcnt vmcnt(0) lgkmcnt(0)
	v_mul_hi_u32 v1, v7, v1
	v_mul_lo_u32 v8, v1, v6
	v_sub_u32_e32 v8, v7, v8
	v_cmp_ge_u32_e32 vcc, v8, v6
	v_add_u32_e32 v9, 1, v1
	s_nop 0
	v_cndmask_b32_e32 v1, v1, v9, vcc
	v_sub_u32_e32 v9, v8, v6
	v_cndmask_b32_e32 v8, v8, v9, vcc
	v_cmp_ge_u32_e32 vcc, v8, v6
	v_add_u32_e32 v8, 1, v1
	s_nop 0
	v_cndmask_b32_e32 v1, v1, v8, vcc
	v_add_u32_e32 v8, 1, v7
	v_mad_u64_u32 v[6:7], s[0:1], v6, v1, v[6:7]
	v_cmp_ne_u32_e32 vcc, v8, v6
	s_and_saveexec_b64 s[0:1], vcc
	s_xor_b64 s[0:1], exec, s[0:1]
	s_cbranch_execz .LBB0_1371
	v_sub_u32_e32 v2, v6, v8
	v_lshlrev_b32_e64 v2, v2, 1
	v_and_b32_e32 v2, 0x10010, v2
	v_cmp_ne_u32_e32 vcc, 0, v2
	s_cbranch_vccz .Lewb_8
	buffer_wbl2 sc1

.LBB0_1738:
	s_lshl_b32 s18, s33, 6
	s_add_i32 s92, s18, 0x500
	s_lshl_b64 s[0:1], s[92:93], 2
	v_lshl_add_u64 v[8:9], v[4:5], 0, s[0:1]
	v_mov_b32_e32 v1, 1
	flat_atomic_add v7, v[8:9], v1 sc0
	v_cvt_f32_u32_e32 v1, v6
	v_sub_u32_e32 v8, 0, v6
	v_rcp_iflag_f32_e32 v1, v1
	s_nop 0
	v_mul_f32_e32 v1, 0x4f7ffffe, v1
	v_cvt_u32_f32_e32 v1, v1
	v_mul_lo_u32 v8, v8, v1
	v_mul_hi_u32 v8, v1, v8
	v_add_u32_e32 v1, v1, v8
	s_waitcnt vmcnt(0) lgkmcnt(0)
	v_mul_hi_u32 v1, v7, v1
	v_mul_lo_u32 v8, v1, v6
	v_sub_u32_e32 v8, v7, v8
	v_cmp_ge_u32_e32 vcc, v8, v6
	v_add_u32_e32 v9, 1, v1
	s_nop 0
	v_cndmask_b32_e32 v1, v1, v9, vcc
	v_sub_u32_e32 v9, v8, v6
	v_cndmask_b32_e32 v8, v8, v9, vcc
	v_cmp_ge_u32_e32 vcc, v8, v6
	v_add_u32_e32 v8, 1, v1
	s_nop 0
	v_cndmask_b32_e32 v1, v1, v8, vcc
	v_add_u32_e32 v8, 1, v7
	v_mad_u64_u32 v[6:7], s[0:1], v6, v1, v[6:7]
	v_cmp_ne_u32_e32 vcc, v8, v6
	s_and_saveexec_b64 s[0:1], vcc
	s_xor_b64 s[0:1], exec, s[0:1]
	v_readlane_b32 s26, v255, 25
	s_cbranch_execz .LBB0_1751
	v_sub_u32_e32 v2, v6, v8
	v_lshlrev_b32_e64 v2, v2, 1
	v_and_b32_e32 v2, 0x10010, v2
	v_cmp_ne_u32_e32 vcc, 0, v2
	s_cbranch_vccz .Lewb_11
	buffer_wbl2 sc1
